# attention loop: s_setprio 3 during X (MFMA) phase, back to static 0/1 for Y (on top of peel)
# speedup vs baseline: 1.0008x; 1.0008x over previous
.LBB0_532:
	s_setprio 3
	s_add_i32 s10, s55, 1
	s_cmp_lg_u32 s55, 2
	s_cselect_b32 s39, s10, 0
	s_lshl_b32 s10, s39, 14
	s_lshl_b32 s44, s55, 14
	s_add_i32 s11, s10, 0x4000
	s_cmp_lg_u32 s39, 2
	s_cselect_b32 s11, s11, 0
	v_add_u32_e32 v2, s11, v232
	ds_read_b64_tr_b16 v[110:111], v2 offset:0
	ds_read_b64_tr_b16 v[112:113], v2 offset:0x800
	ds_read_b64_tr_b16 v[106:107], v2 offset:0x1000
	ds_read_b64_tr_b16 v[108:109], v2 offset:0x1800
	ds_read_b64_tr_b16 v[102:103], v2 offset:0x2000
	ds_read_b64_tr_b16 v[104:105], v2 offset:0x2800
	ds_read_b64_tr_b16 v[98:99], v2 offset:0x3000
	ds_read_b64_tr_b16 v[100:101], v2 offset:0x3800
	v_add_u32_e32 v12, s44, v225
	ds_read_b128 v[4:7], v12 offset:0
	ds_read_b128 v[8:11], v12 offset:0x2000
	v_add_u32_e32 v16, s44, v226
	ds_read_b128 v[170:173], v16 offset:0
	ds_read_b128 v[12:15], v16 offset:0x2000
	v_add_u32_e32 v16, s44, v227
	ds_read_b128 v[174:177], v16 offset:0
	ds_read_b128 v[162:165], v16 offset:0x2000
	v_add_u32_e32 v16, s44, v228
	ds_read_b128 v[178:181], v16 offset:0
	s_add_i32 s44, s38, 2
	ds_read_b128 v[166:169], v16 offset:0x2000
	s_cmp_ge_i32 s44, s35
	s_cselect_b64 s[96:97], -1, 0
	s_and_b64 vcc, exec, s[96:97]
	s_cbranch_vccnz .LBB0_534
	s_add_i32 s11, s34, s11
	v_lshl_add_u64 v[16:17], s[94:95], 0, v[208:209]
	s_add_i32 m0, s11, 0xc000
	s_nop 0
	global_load_lds_dwordx4 v[16:17], off
	v_lshl_add_u64 v[16:17], s[94:95], 0, v[210:211]
	s_add_i32 m0, s11, 0xc400
	s_nop 0
	global_load_lds_dwordx4 v[16:17], off

.LBB0_536:
	s_waitcnt lgkmcnt(8)
	v_mfma_f32_32x32x16_bf16 v[114:129], v[4:7], v[130:133], v[18:33]
	v_mfma_f32_32x32x16_bf16 v[98:113], v[8:11], v[130:133], v[18:33]
	v_mfma_f32_32x32x16_bf16 v[114:129], v[170:173], v[134:137], v[114:129]
	v_mfma_f32_32x32x16_bf16 v[98:113], v[12:15], v[134:137], v[98:113]
	v_mfma_f32_32x32x16_bf16 v[114:129], v[174:177], v[138:141], v[114:129]
	v_mfma_f32_32x32x16_bf16 v[98:113], v[162:165], v[138:141], v[98:113]
	v_mfma_f32_32x32x16_bf16 v[114:129], v[178:181], v[142:145], v[114:129]
	v_mfma_f32_32x32x16_bf16 v[98:113], v[166:169], v[142:145], v[98:113]
	ds_read_b64_tr_b16 v[4:5], v2 offset:0x400
	ds_read_b64_tr_b16 v[6:7], v2 offset:0xc00
	ds_read_b64_tr_b16 v[8:9], v2 offset:0x1400
	ds_read_b64_tr_b16 v[10:11], v2 offset:0x1c00
	ds_read_b64_tr_b16 v[12:13], v2 offset:0x2400
	ds_read_b64_tr_b16 v[14:15], v2 offset:0x2c00
	ds_read_b64_tr_b16 v[162:163], v2 offset:0x3400
	ds_read_b64_tr_b16 v[164:165], v2 offset:0x3c00
	s_waitcnt lgkmcnt(8)
	v_mfma_f32_32x32x16_bf16 v[66:81], v[146:149], v[194:197], v[66:81]
	v_mfma_f32_32x32x16_bf16 v[66:81], v[150:153], v[190:193], v[66:81]
	v_mfma_f32_32x32x16_bf16 v[66:81], v[154:157], v[186:189], v[66:81]
	v_mfma_f32_32x32x16_bf16 v[66:81], v[158:161], v[182:185], v[66:81]
	ds_read_b64_tr_b16 v[166:167], v2 offset:0x600
	ds_read_b64_tr_b16 v[168:169], v2 offset:0xe00
	ds_read_b64_tr_b16 v[170:171], v2 offset:0x1600
	ds_read_b64_tr_b16 v[172:173], v2 offset:0x1e00
	ds_read_b64_tr_b16 v[174:175], v2 offset:0x2600
	ds_read_b64_tr_b16 v[176:177], v2 offset:0x2e00
	ds_read_b64_tr_b16 v[178:179], v2 offset:0x3600
	ds_read_b64_tr_b16 v[180:181], v2 offset:0x3e00
	s_waitcnt lgkmcnt(8)
	v_mfma_f32_32x32x16_bf16 v[50:65], v[146:149], v[4:7], v[50:65]
	v_mfma_f32_32x32x16_bf16 v[50:65], v[150:153], v[8:11], v[50:65]
	v_mfma_f32_32x32x16_bf16 v[50:65], v[154:157], v[12:15], v[50:65]
	v_mfma_f32_32x32x16_bf16 v[50:65], v[158:161], v[162:165], v[50:65]
	s_waitcnt lgkmcnt(0)
	v_mfma_f32_32x32x16_bf16 v[34:49], v[146:149], v[166:169], v[34:49]
	v_mfma_f32_32x32x16_bf16 v[34:49], v[150:153], v[170:173], v[34:49]
	v_mfma_f32_32x32x16_bf16 v[34:49], v[154:157], v[174:177], v[34:49]
	v_mfma_f32_32x32x16_bf16 v[34:49], v[158:161], v[178:181], v[34:49]
	s_setprio 0
	s_and_b64 vcc, exec, s[6:7]
	s_cbranch_vccnz .LBB0_541
	s_setprio 1
	s_mov_b64 s[10:11], -1
	s_and_b64 vcc, exec, s[96:97]
	s_cbranch_vccz .LBB0_539
	s_waitcnt vmcnt(0)
	s_mov_b64 s[10:11], 0
